# v36 + next-unit L2 warm-up lines of the gate/up weights split between sibling workgroups (pm 0,1 touch K-tiles 0-1, pm 2,3 touch K-tiles 2-3)
# speedup vs baseline: 1.0053x; 1.0053x over previous
.LBB0_1422:
	s_mul_i32 s4, s72, s11
	s_add_i32 s6, s4, s49
	s_cmp_eq_u32 s11, 5
	s_cselect_b64 s[4:5], -1, 0
	s_and_b64 s[24:25], s[76:77], s[4:5]
	s_add_i32 s7, s6, 0xffffff80
	s_and_b64 s[4:5], s[24:25], s[12:13]
	s_and_b64 s[4:5], s[4:5], exec
	s_cselect_b32 s30, s7, s6
	s_cmpk_gt_i32 s30, 0x57f
	s_cbranch_scc1 .LBB0_1457
	s_cmp_lt_u32 s11, 5
	s_cselect_b64 s[4:5], -1, 0
	s_and_b64 s[26:27], s[76:77], s[4:5]
	v_cndmask_b32_e64 v2, 0, 1, s[26:27]
	v_mov_b64_e32 v[184:185], 0
	v_cmp_ne_u32_e64 s[6:7], 1, v2
	s_andn2_b64 vcc, exec, s[26:27]
	v_mov_b32_e32 v204, v208
	v_mov_b32_e32 v205, v209
	v_mov_b32_e32 v206, v210
	v_mov_b32_e32 v207, v211
	v_mov_b64_e32 v[186:187], 0
	v_mov_b64_e32 v[188:189], 0
	s_cbranch_vccnz .LBB0_1425
	s_add_i32 s28, s11, 1
	s_lshl_b32 s4, s28, 8
	s_add_i32 s29, s4, s50
	s_add_i32 s31, s29, 0xffffff80
	s_and_b64 s[4:5], s[14:15], exec
	s_cselect_b32 s4, s29, s31
	s_cmp_eq_u32 s28, 5
	s_cselect_b32 s4, s4, s29
	s_cselect_b32 s28, s42, 0
	s_ashr_i32 s29, s4, 2
	s_mul_hi_i32 s5, s29, 0x2e8ba2e9
	s_lshl_b32 s4, s4, 8
	s_lshr_b32 s31, s5, 31
	s_ashr_i32 s5, s5, 2
	s_and_b32 s4, s4, 0x300
	s_add_i32 s5, s5, s31
	v_add_u32_e32 v2, s4, v195
	s_waitcnt vmcnt(6)
	v_lshrrev_b32_e32 v12, 8, v2
	s_lshl_b32 s31, s5, 8
	s_lshl_b32 s33, s4, 4
	v_add_u32_e32 v10, s4, v202
	v_lshl_add_u32 v2, v12, 12, s31
	s_add_i32 s33, s33, s31
	v_or_b32_e32 v6, 64, v171
	v_lshrrev_b32_e32 v13, 8, v10
	v_or_b32_e32 v2, v2, v195
	v_or_b32_e32 v4, s33, v171
	v_or_b32_e32 v6, s33, v6
	v_lshl_add_u32 v10, v13, 12, s31
	v_ashrrev_i32_e32 v3, 31, v2
	v_ashrrev_i32_e32 v5, 31, v4
	v_ashrrev_i32_e32 v7, 31, v6
	v_or_b32_e32 v8, s33, v191
	v_or_b32_e32 v10, v10, v202
	v_lshl_add_u64 v[2:3], v[2:3], 2, s[16:17]
	v_lshl_add_u64 v[4:5], v[4:5], 2, s[16:17]
	v_lshl_add_u64 v[6:7], v[6:7], 2, s[16:17]
	v_ashrrev_i32_e32 v9, 31, v8
	v_ashrrev_i32_e32 v11, 31, v10
	v_lshl_add_u64 v[8:9], v[8:9], 2, s[16:17]
	v_lshl_add_u64 v[10:11], v[10:11], 2, s[16:17]
	global_load_dword v14, v[2:3], off
	s_nop 0
	global_load_dword v4, v[4:5], off
	s_nop 0
	global_load_dword v5, v[6:7], off
	s_nop 0
	global_load_dword v6, v[8:9], off
	global_load_dword v7, v[10:11], off
	v_lshrrev_b32_e32 v2, 2, v0
	v_mov_b32_e32 v3, 0x1600000
	v_lshlrev_b32_e32 v9, 22, v13
	v_add_u32_e32 v8, s28, v2
	s_lshl_b32 s31, s4, 14
	s_mul_i32 s33, s5, 22
	v_mad_i64_i32 v[2:3], s[4:5], s5, v3, v[176:177]
	s_sub_i32 s4, s29, s33
	s_lshl_b32 s4, s4, 7
	s_ashr_i32 s5, s4, 31
	v_mov_b32_e32 v181, v173
	s_waitcnt vmcnt(4)
	v_lshlrev_b32_e32 v10, 11, v14
	s_waitcnt vmcnt(3)
	v_lshl_add_u32 v4, v4, 11, s31
	s_waitcnt vmcnt(2)
	v_lshl_add_u32 v5, v5, 11, s31
	s_waitcnt vmcnt(1)
	v_lshl_add_u32 v6, v6, 11, s31
	s_waitcnt vmcnt(0)
	v_lshl_add_u32 v7, v7, 11, v9
	v_lshl_add_u32 v9, v12, 22, v10
	v_or_b32_e32 v172, s28, v9
	v_lshl_add_u64 v[184:185], v[172:173], 1, v[174:175]
	v_mul_u32_u24_e32 v172, 0x2c00, v8
	v_lshl_add_u64 v[2:3], v[2:3], 0, v[172:173]
	v_lshl_add_u64 v[2:3], s[4:5], 2, v[2:3]
	v_or3_b32 v4, v4, v201, s28
	v_or3_b32 v5, v5, v201, s28
	v_or3_b32 v6, v6, v201, s28
	v_or3_b32 v7, v7, v201, s28
	v_lshl_add_u64 v[186:187], v[2:3], 0, v[180:181]
	v_lshlrev_b32_e32 v204, 1, v4
	v_lshlrev_b32_e32 v205, 1, v5
	v_lshlrev_b32_e32 v206, 1, v6
	v_lshlrev_b32_e32 v207, 1, v7
	s_bfe_u32 s4, s96, 0x10004
	s_mul_i32 s4, s4, 0x160000
	s_mov_b32 s5, 0
	v_lshl_add_u64 v[186:187], s[4:5], 0, v[186:187]
	v_lshl_add_u64 v[188:189], v[186:187], 0, s[20:21]
